# peel+trim+tmax + relu without the canonicalising v_max in the MLP-up epilogue
# speedup vs baseline: 1.0118x; 1.0089x over previous
.LBB0_1390:
	s_lshl_b32 s4, s64, 8
	s_or_b32 s4, s4, s60
	v_max_f32_e32 v129, 0, v129
	v_lshl_or_b32 v162, v162, 3, s4
	v_max_f32_e32 v128, 0, v128
	v_ashrrev_i32_e32 v163, 31, v162
	v_lshlrev_b64 v[158:159], 13, v[158:159]
	v_max_f32_e32 v125, 0, v125
	v_lshl_add_u64 v[164:165], s[14:15], 0, v[158:159]
	v_lshlrev_b64 v[158:159], 1, v[162:163]
	v_max_f32_e32 v124, 0, v124
	v_lshl_add_u64 v[162:163], v[164:165], 0, v[158:159]
	v_pk_mul_f32 v[164:165], v[124:125], v[124:125]
	v_max_f32_e32 v125, 0, v131
	v_max_f32_e32 v124, 0, v130
	v_pk_mul_f32 v[130:131], v[124:125], v[124:125]
	v_max_f32_e32 v125, 0, v127
	v_max_f32_e32 v124, 0, v126
	v_max_f32_e32 v121, 0, v121
	v_max_f32_e32 v120, 0, v120
	v_pk_mul_f32 v[128:129], v[128:129], v[128:129]
	v_pk_mul_f32 v[166:167], v[124:125], v[124:125]
	v_max_f32_e32 v117, 0, v117
	v_cvt_pk_bf16_f32 v124, v128, v129
	v_cvt_pk_bf16_f32 v125, v130, v131
	v_cvt_pk_bf16_f32 v126, v164, v165
	v_cvt_pk_bf16_f32 v127, v166, v167
	v_max_f32_e32 v116, 0, v116
	global_store_dwordx4 v[162:163], v[124:127], off
	v_pk_mul_f32 v[120:121], v[120:121], v[120:121]
	s_andn2_b64 vcc, exec, s[38:39]
	v_pk_mul_f32 v[124:125], v[116:117], v[116:117]
	v_max_f32_e32 v117, 0, v123
	v_max_f32_e32 v116, 0, v122
	v_pk_mul_f32 v[122:123], v[116:117], v[116:117]
	v_max_f32_e32 v117, 0, v119
	v_max_f32_e32 v116, 0, v118
	v_max_f32_e32 v113, 0, v113
	v_max_f32_e32 v112, 0, v112
	v_pk_mul_f32 v[126:127], v[116:117], v[116:117]
	v_max_f32_e32 v109, 0, v109
	v_cvt_pk_bf16_f32 v116, v120, v121
	v_cvt_pk_bf16_f32 v117, v122, v123
	v_cvt_pk_bf16_f32 v118, v124, v125
	v_cvt_pk_bf16_f32 v119, v126, v127
	v_max_f32_e32 v108, 0, v108
	global_store_dwordx4 v[162:163], v[116:119], off offset:256
	v_pk_mul_f32 v[112:113], v[112:113], v[112:113]
	s_mov_b64 s[4:5], -1
	v_pk_mul_f32 v[118:119], v[108:109], v[108:109]
	v_max_f32_e32 v109, 0, v115
	v_max_f32_e32 v108, 0, v114
	v_pk_mul_f32 v[114:115], v[108:109], v[108:109]
	v_max_f32_e32 v109, 0, v111
	v_max_f32_e32 v108, 0, v110
	v_max_f32_e32 v105, 0, v105
	v_lshlrev_b64 v[116:117], 13, v[156:157]
	v_max_f32_e32 v104, 0, v104
	v_lshl_add_u64 v[116:117], s[14:15], 0, v[116:117]
	v_pk_mul_f32 v[120:121], v[108:109], v[108:109]
	v_max_f32_e32 v101, 0, v101
	v_lshl_add_u64 v[116:117], v[116:117], 0, v[158:159]
	v_cvt_pk_bf16_f32 v108, v112, v113
	v_cvt_pk_bf16_f32 v109, v114, v115
	v_cvt_pk_bf16_f32 v110, v118, v119
	v_cvt_pk_bf16_f32 v111, v120, v121
	v_max_f32_e32 v100, 0, v100
	global_store_dwordx4 v[116:117], v[108:111], off
	v_pk_mul_f32 v[104:105], v[104:105], v[104:105]
	s_nop 0
	v_pk_mul_f32 v[108:109], v[100:101], v[100:101]
	v_max_f32_e32 v101, 0, v107
	v_max_f32_e32 v100, 0, v106
	v_pk_mul_f32 v[106:107], v[100:101], v[100:101]
	v_max_f32_e32 v101, 0, v103
	v_max_f32_e32 v100, 0, v102
	v_max_f32_e32 v97, 0, v97
	v_max_f32_e32 v96, 0, v96
	v_pk_mul_f32 v[110:111], v[100:101], v[100:101]
	v_max_f32_e32 v93, 0, v93
	v_cvt_pk_bf16_f32 v100, v104, v105
	v_cvt_pk_bf16_f32 v101, v106, v107
	v_cvt_pk_bf16_f32 v102, v108, v109
	v_cvt_pk_bf16_f32 v103, v110, v111
	v_max_f32_e32 v92, 0, v92
	global_store_dwordx4 v[116:117], v[100:103], off offset:256
	v_pk_mul_f32 v[96:97], v[96:97], v[96:97]
	s_nop 0
	v_pk_mul_f32 v[102:103], v[92:93], v[92:93]
	v_max_f32_e32 v93, 0, v99
	v_max_f32_e32 v92, 0, v98
	v_pk_mul_f32 v[98:99], v[92:93], v[92:93]
	v_max_f32_e32 v93, 0, v95
	v_max_f32_e32 v92, 0, v94
	v_max_f32_e32 v89, 0, v89
	v_lshlrev_b64 v[100:101], 13, v[154:155]
	v_max_f32_e32 v88, 0, v88
	v_lshl_add_u64 v[100:101], s[14:15], 0, v[100:101]
	v_pk_mul_f32 v[104:105], v[92:93], v[92:93]
	v_max_f32_e32 v85, 0, v85
	v_lshl_add_u64 v[100:101], v[100:101], 0, v[158:159]
	v_cvt_pk_bf16_f32 v92, v96, v97
	v_cvt_pk_bf16_f32 v93, v98, v99
	v_cvt_pk_bf16_f32 v94, v102, v103
	v_cvt_pk_bf16_f32 v95, v104, v105
	v_max_f32_e32 v84, 0, v84
	global_store_dwordx4 v[100:101], v[92:95], off
	v_pk_mul_f32 v[88:89], v[88:89], v[88:89]
	s_nop 0
	v_pk_mul_f32 v[92:93], v[84:85], v[84:85]
	v_max_f32_e32 v85, 0, v91
	v_max_f32_e32 v84, 0, v90
	v_pk_mul_f32 v[90:91], v[84:85], v[84:85]
	v_max_f32_e32 v85, 0, v87
	v_max_f32_e32 v84, 0, v86
	v_max_f32_e32 v81, 0, v81
	v_max_f32_e32 v80, 0, v80
	v_pk_mul_f32 v[94:95], v[84:85], v[84:85]
	v_max_f32_e32 v77, 0, v77
	v_cvt_pk_bf16_f32 v84, v88, v89
	v_cvt_pk_bf16_f32 v85, v90, v91
	v_cvt_pk_bf16_f32 v86, v92, v93
	v_cvt_pk_bf16_f32 v87, v94, v95
	v_max_f32_e32 v76, 0, v76
	global_store_dwordx4 v[100:101], v[84:87], off offset:256
	v_pk_mul_f32 v[80:81], v[80:81], v[80:81]
	s_nop 0
	v_pk_mul_f32 v[86:87], v[76:77], v[76:77]
	v_max_f32_e32 v77, 0, v83
	v_max_f32_e32 v76, 0, v82
	v_pk_mul_f32 v[82:83], v[76:77], v[76:77]
	v_max_f32_e32 v77, 0, v79
	v_max_f32_e32 v76, 0, v78
	v_max_f32_e32 v73, 0, v73
	v_lshlrev_b64 v[84:85], 13, v[152:153]
	v_max_f32_e32 v72, 0, v72
	v_lshl_add_u64 v[84:85], s[14:15], 0, v[84:85]
	v_pk_mul_f32 v[88:89], v[76:77], v[76:77]
	v_max_f32_e32 v69, 0, v69
	v_lshl_add_u64 v[84:85], v[84:85], 0, v[158:159]
	v_cvt_pk_bf16_f32 v76, v80, v81
	v_cvt_pk_bf16_f32 v77, v82, v83
	v_cvt_pk_bf16_f32 v78, v86, v87
	v_cvt_pk_bf16_f32 v79, v88, v89
	v_max_f32_e32 v68, 0, v68
	global_store_dwordx4 v[84:85], v[76:79], off
	v_pk_mul_f32 v[72:73], v[72:73], v[72:73]
	s_nop 0
	v_pk_mul_f32 v[76:77], v[68:69], v[68:69]
	v_max_f32_e32 v69, 0, v75
	v_max_f32_e32 v68, 0, v74
	v_pk_mul_f32 v[74:75], v[68:69], v[68:69]
	v_max_f32_e32 v69, 0, v71
	v_max_f32_e32 v68, 0, v70
	v_max_f32_e32 v65, 0, v65
	v_max_f32_e32 v64, 0, v64
	v_pk_mul_f32 v[78:79], v[68:69], v[68:69]
	v_max_f32_e32 v61, 0, v61
	v_cvt_pk_bf16_f32 v68, v72, v73
	v_cvt_pk_bf16_f32 v69, v74, v75
	v_cvt_pk_bf16_f32 v70, v76, v77
	v_cvt_pk_bf16_f32 v71, v78, v79
	v_max_f32_e32 v60, 0, v60
	global_store_dwordx4 v[84:85], v[68:71], off offset:256
	v_pk_mul_f32 v[64:65], v[64:65], v[64:65]
	s_nop 0
	v_pk_mul_f32 v[70:71], v[60:61], v[60:61]
	v_max_f32_e32 v61, 0, v67
	v_max_f32_e32 v60, 0, v66
	v_pk_mul_f32 v[66:67], v[60:61], v[60:61]
	v_max_f32_e32 v61, 0, v63
	v_max_f32_e32 v60, 0, v62
	v_max_f32_e32 v57, 0, v57
	v_lshlrev_b64 v[68:69], 13, v[150:151]
	v_max_f32_e32 v56, 0, v56
	v_lshl_add_u64 v[68:69], s[14:15], 0, v[68:69]
	v_pk_mul_f32 v[72:73], v[60:61], v[60:61]
	v_max_f32_e32 v53, 0, v53
	v_lshl_add_u64 v[68:69], v[68:69], 0, v[158:159]
	v_cvt_pk_bf16_f32 v60, v64, v65
	v_cvt_pk_bf16_f32 v61, v66, v67
	v_cvt_pk_bf16_f32 v62, v70, v71
	v_cvt_pk_bf16_f32 v63, v72, v73
	v_max_f32_e32 v52, 0, v52
	global_store_dwordx4 v[68:69], v[60:63], off
	v_pk_mul_f32 v[56:57], v[56:57], v[56:57]
	s_nop 0
	v_pk_mul_f32 v[60:61], v[52:53], v[52:53]
	v_max_f32_e32 v53, 0, v59
	v_max_f32_e32 v52, 0, v58
	v_pk_mul_f32 v[58:59], v[52:53], v[52:53]
	v_max_f32_e32 v53, 0, v55
	v_max_f32_e32 v52, 0, v54
	v_max_f32_e32 v49, 0, v49
	v_max_f32_e32 v48, 0, v48
	v_pk_mul_f32 v[62:63], v[52:53], v[52:53]
	v_max_f32_e32 v45, 0, v45
	v_cvt_pk_bf16_f32 v52, v56, v57
	v_cvt_pk_bf16_f32 v53, v58, v59
	v_cvt_pk_bf16_f32 v54, v60, v61
	v_cvt_pk_bf16_f32 v55, v62, v63
	v_max_f32_e32 v44, 0, v44
	global_store_dwordx4 v[68:69], v[52:55], off offset:256
	v_pk_mul_f32 v[48:49], v[48:49], v[48:49]
	s_nop 0
	v_pk_mul_f32 v[54:55], v[44:45], v[44:45]
	v_max_f32_e32 v45, 0, v51
	v_max_f32_e32 v44, 0, v50
	v_pk_mul_f32 v[50:51], v[44:45], v[44:45]
	v_max_f32_e32 v45, 0, v47
	v_max_f32_e32 v44, 0, v46
	v_max_f32_e32 v41, 0, v41
	v_lshlrev_b64 v[52:53], 13, v[148:149]
	v_max_f32_e32 v40, 0, v40
	v_lshl_add_u64 v[52:53], s[14:15], 0, v[52:53]
	v_pk_mul_f32 v[56:57], v[44:45], v[44:45]
	v_max_f32_e32 v37, 0, v37
	v_lshl_add_u64 v[52:53], v[52:53], 0, v[158:159]
	v_cvt_pk_bf16_f32 v44, v48, v49
	v_cvt_pk_bf16_f32 v45, v50, v51
	v_cvt_pk_bf16_f32 v46, v54, v55
	v_cvt_pk_bf16_f32 v47, v56, v57
	v_max_f32_e32 v36, 0, v36
	global_store_dwordx4 v[52:53], v[44:47], off
	v_pk_mul_f32 v[40:41], v[40:41], v[40:41]
	s_nop 0
	v_pk_mul_f32 v[44:45], v[36:37], v[36:37]
	v_max_f32_e32 v37, 0, v43
	v_max_f32_e32 v36, 0, v42
	v_pk_mul_f32 v[42:43], v[36:37], v[36:37]
	v_max_f32_e32 v37, 0, v39
	v_max_f32_e32 v36, 0, v38
	v_max_f32_e32 v33, 0, v33
	v_max_f32_e32 v32, 0, v32
	v_pk_mul_f32 v[46:47], v[36:37], v[36:37]
	v_max_f32_e32 v29, 0, v29
	v_cvt_pk_bf16_f32 v36, v40, v41
	v_cvt_pk_bf16_f32 v37, v42, v43
	v_cvt_pk_bf16_f32 v38, v44, v45
	v_cvt_pk_bf16_f32 v39, v46, v47
	v_max_f32_e32 v28, 0, v28
	global_store_dwordx4 v[52:53], v[36:39], off offset:256
	v_pk_mul_f32 v[32:33], v[32:33], v[32:33]
	s_nop 0
	v_pk_mul_f32 v[38:39], v[28:29], v[28:29]
	v_max_f32_e32 v29, 0, v35
	v_max_f32_e32 v28, 0, v34
	v_pk_mul_f32 v[34:35], v[28:29], v[28:29]
	v_max_f32_e32 v29, 0, v31
	v_max_f32_e32 v28, 0, v30
	v_max_f32_e32 v25, 0, v25
	v_lshlrev_b64 v[36:37], 13, v[146:147]
	v_max_f32_e32 v24, 0, v24
	v_lshl_add_u64 v[36:37], s[14:15], 0, v[36:37]
	v_pk_mul_f32 v[40:41], v[28:29], v[28:29]
	v_max_f32_e32 v21, 0, v21
	v_lshl_add_u64 v[36:37], v[36:37], 0, v[158:159]
	v_cvt_pk_bf16_f32 v28, v32, v33
	v_cvt_pk_bf16_f32 v29, v34, v35
	v_cvt_pk_bf16_f32 v30, v38, v39
	v_cvt_pk_bf16_f32 v31, v40, v41
	v_max_f32_e32 v20, 0, v20
	global_store_dwordx4 v[36:37], v[28:31], off
	v_pk_mul_f32 v[24:25], v[24:25], v[24:25]
	s_nop 0
	v_pk_mul_f32 v[28:29], v[20:21], v[20:21]
	v_max_f32_e32 v21, 0, v27
	v_max_f32_e32 v20, 0, v26
	v_pk_mul_f32 v[26:27], v[20:21], v[20:21]
	v_max_f32_e32 v21, 0, v23
	v_max_f32_e32 v20, 0, v22
	v_max_f32_e32 v17, 0, v17
	v_max_f32_e32 v16, 0, v16
	v_pk_mul_f32 v[30:31], v[20:21], v[20:21]
	v_max_f32_e32 v13, 0, v13
	v_cvt_pk_bf16_f32 v20, v24, v25
	v_cvt_pk_bf16_f32 v21, v26, v27
	v_cvt_pk_bf16_f32 v22, v28, v29
	v_cvt_pk_bf16_f32 v23, v30, v31
	v_max_f32_e32 v12, 0, v12
	global_store_dwordx4 v[36:37], v[20:23], off offset:256
	v_pk_mul_f32 v[16:17], v[16:17], v[16:17]
	s_nop 0
	v_pk_mul_f32 v[22:23], v[12:13], v[12:13]
	v_max_f32_e32 v13, 0, v19
	v_max_f32_e32 v12, 0, v18
	v_pk_mul_f32 v[18:19], v[12:13], v[12:13]
	v_max_f32_e32 v13, 0, v15
	v_max_f32_e32 v12, 0, v14
	v_max_f32_e32 v9, 0, v9
	v_lshlrev_b64 v[20:21], 13, v[144:145]
	v_max_f32_e32 v8, 0, v8
	v_lshl_add_u64 v[20:21], s[14:15], 0, v[20:21]
	v_pk_mul_f32 v[24:25], v[12:13], v[12:13]
	v_max_f32_e32 v5, 0, v5
	v_lshl_add_u64 v[20:21], v[20:21], 0, v[158:159]
	v_cvt_pk_bf16_f32 v12, v16, v17
	v_cvt_pk_bf16_f32 v13, v18, v19
	v_cvt_pk_bf16_f32 v14, v22, v23
	v_cvt_pk_bf16_f32 v15, v24, v25
	v_max_f32_e32 v4, 0, v4
	global_store_dwordx4 v[20:21], v[12:15], off
	v_pk_mul_f32 v[8:9], v[8:9], v[8:9]
	s_nop 0
	v_pk_mul_f32 v[12:13], v[4:5], v[4:5]
	v_max_f32_e32 v5, 0, v11
	v_max_f32_e32 v4, 0, v10
	v_pk_mul_f32 v[10:11], v[4:5], v[4:5]
	v_max_f32_e32 v5, 0, v7
	v_max_f32_e32 v4, 0, v6
	v_pk_mul_f32 v[14:15], v[4:5], v[4:5]
	v_cvt_pk_bf16_f32 v4, v8, v9
	v_cvt_pk_bf16_f32 v5, v10, v11
	v_cvt_pk_bf16_f32 v6, v12, v13
	v_cvt_pk_bf16_f32 v7, v14, v15
	global_store_dwordx4 v[20:21], v[4:7], off offset:256
	s_cbranch_vccnz .LBB0_1372
	s_andn2_b64 vcc, exec, s[10:11]
	s_cbranch_vccnz .LBB0_1371
	s_barrier
	s_branch .LBB0_1371
